# W_in phase: converting workgroups keep taking queue entries until the first GEMM workgroup finishes its last tile (GEMM workgroups post a second arrival), not until 16 have started it
# baseline (speedup 1.0000x reference)
; __device__ __forceinline__ unsigned xb_add(unsigned* p, unsigned v) { return __hip_atomic_fetch_add(p, v, __ATOMIC_RELAXED, __HIP_MEMORY_SCOPE_AGENT); }
; __device__ __forceinline__ unsigned convq_take(unsigned* ctl, bool allow2) {
;     unsigned it = xb_add(ctl + CW_Q, 1u); if (it < (unsigned)CQ_M13) return it;
;     if (allow2) { it = xb_add(ctl + CW_Q + 32, 1u); if (it < (unsigned)CQ_M2) return 0x80000000u | it; }
;     return CQ_END;
; }
;     int tid = threadIdx.x; asm volatile("" : "+v"(tid)); const int lane = tid & 63, wave = __builtin_amdgcn_readfirstlane(tid >> 6);
;     unsigned nxt = CQ_END; int left = quota;
;     ...
;     int par = 0;
; #pragma unroll 1
;     for (;;) {
;         if (tid == 0) bc[par] = nxt;
;         __syncthreads();
;         const unsigned cur = __builtin_amdgcn_readfirstlane(bc[par]); par ^= 2;
;         if (cur == CQ_END) break;
.LBB0_145:
	s_or_b64 exec, exec, s[10:11]
	s_waitcnt vmcnt(0)
	v_cmp_gt_u32_e32 vcc, 0xe1, v6
	s_nop 1
	v_cndmask_b32_e32 v1, 1, v1, vcc
	v_readfirstlane_b32 s10, v3
	s_nop 1
	v_add_u32_e32 v129, s10, v2
	s_movk_i32 s10, 0xdff
	v_cmp_lt_u32_e32 vcc, s10, v129
	s_and_saveexec_b64 s[10:11], vcc
	s_cbranch_execz .LBB0_149
	s_mov_b64 s[16:17], exec
	v_mbcnt_lo_u32_b32 v2, s16, 0
	v_mbcnt_hi_u32_b32 v2, s17, v2
	v_cmp_eq_u32_e32 vcc, 0, v2
	s_and_saveexec_b64 s[12:13], vcc
	s_cbranch_execz .LBB0_148
	s_bcnt1_i32_b64 s14, s[16:17]
	v_mov_b32_e32 v3, s14
	v_readlane_b32 s14, v250, 20
	v_readlane_b32 s15, v250, 21
	s_nop 4
	global_atomic_add v3, v187, v3, s[14:15] sc0

; __global__ void __launch_bounds__(NWAVES * 64, 2) trunk_fwd(Args args) {
;     ...
;             if (bx < gg) {
;                 pg8::Gemm g{Hb, WIN_T + (size_t)layer * ZLD * D, M, ZLD, D, 0}; pg8::StaticOrder S; S.init(M, ZLD, gg, bx);
;                 pg8::EpiWin E{Zb, FLAT};
;                 pg8::gemm_phase(lds, g, S, E, tz, ctl + CW_DONE(layer * 3 + 0));
;             } else conv_run(args.in[I_M1], args.in[I_M3], args.in[I_M2], MUP_T, MDN_T, ctl, MISC + 16, true, ctl + CW_DONE(layer * 3 + 0), 16u, 1 << 30, 1);
.Lwin_end_sig:
	s_and_b64 vcc, exec, s[6:7]
	s_cbranch_vccnz .LBB0_202
	v_cmp_eq_u32_e32 vcc, 0, v228
	s_and_saveexec_b64 s[16:17], vcc
	v_mov_b32_e32 v2, 1
	global_atomic_add v187, v2, s[4:5]
	s_or_b64 exec, exec, s[16:17]
